# MoE prologue row tables: the six weight/rstd gathers of the three units issued together (one round trip instead of three)
# speedup vs baseline: 1.0064x; 1.0064x over previous
; __global__ void __launch_bounds__(512, 2) hymba_fwd(Args args) {
;     ...
;         { int tkv[MAXU], off[MAXU]; bool has[MAXU], vl[MAXU];
; #pragma unroll
;           for (int i = 0; i < MAXU; ++i) { pg8::Unit u; has[i] = S.next(i, u); vl[i] = false; tkv[i] = -1; off[i] = 0;
;               if (has[i] && tid < 256) { const int idx = 256 * u.lt + tid; vl[i] = idx < tb[33 + u.e]; off[i] = u.e * SEQ + idx; if (vl[i]) tkv[i] = ltok[off[i]]; } }
; #pragma unroll
;           for (int i = 0; i < MAXU; ++i) if (has[i] && tid < 256) {
;               mtok[i * 256 + tid] = tkv[i]; mw[i * 256 + tid] = vl[i] ? lw[off[i]] : 0.f; mr[i * 256 + tid] = vl[i] ? ((const float*)(ws + WS_RSTD))[tkv[i]] : 0.f; } }
.LBB0_720:
	s_or_b64 exec, exec, s[16:17]
	s_add_u32 s16, s26, 0x310000
	s_addc_u32 s17, s27, 0
	s_mov_b64 s[18:19], exec
	s_waitcnt vmcnt(0)
	v_lshl_add_u32 v12, v28, 2, 0
	v_add_u32_e32 v12, 0x20000, v12
	v_mov_b32_e32 v1, 0
	v_mov_b32_e32 v3, 0
	v_mov_b32_e32 v5, 0
	v_mov_b32_e32 v7, 0
	v_mov_b32_e32 v9, 0
	v_mov_b32_e32 v11, 0
	s_and_b64 exec, s[18:19], s[6:7]
	ds_write_b32 v12, v2
	s_and_b64 exec, s[18:19], s[10:11]
	ds_write_b32 v12, v6 offset:1024
	s_and_b64 exec, s[18:19], s[12:13]
	ds_write_b32 v12, v10 offset:2048
	s_and_b64 exec, s[18:19], s[8:9]
	v_lshl_add_u64 v[12:13], v[0:1], 2, s[22:23]
	v_lshl_add_u64 v[14:15], v[2:3], 2, s[16:17]
	global_load_dword v1, v[12:13], off
	global_load_dword v3, v[14:15], off
	s_and_b64 exec, s[18:19], s[0:1]
	v_lshl_add_u64 v[12:13], v[4:5], 2, s[22:23]
	v_lshl_add_u64 v[14:15], v[6:7], 2, s[16:17]
	global_load_dword v5, v[12:13], off
	global_load_dword v7, v[14:15], off
	s_and_b64 exec, s[18:19], s[14:15]
	v_lshl_add_u64 v[12:13], v[8:9], 2, s[22:23]
	v_lshl_add_u64 v[14:15], v[10:11], 2, s[16:17]
	global_load_dword v9, v[12:13], off
	global_load_dword v11, v[14:15], off
	s_mov_b64 exec, s[18:19]
	v_lshl_add_u32 v13, v28, 2, 0
	v_add_u32_e32 v14, 0x20c00, v13
	v_add_u32_e32 v15, 0x21800, v13
	s_waitcnt vmcnt(0)
	s_and_b64 exec, s[18:19], s[6:7]
	ds_write_b32 v14, v1
	ds_write_b32 v15, v3
	s_and_b64 exec, s[18:19], s[10:11]
	ds_write_b32 v14, v5 offset:1024
	ds_write_b32 v15, v7 offset:1024
	s_and_b64 exec, s[18:19], s[12:13]
	ds_write_b32 v14, v9 offset:2048
	ds_write_b32 v15, v11 offset:2048
	s_mov_b64 exec, s[18:19]
	s_mov_b64 s[0:1], 0
